# baseline (speedup 1.0000x reference)
.Lfa_tileend:
	s_setprio 2
	ds_read_b128 v[126:129], v137
	ds_read_b128 v[114:117], v138 offset:57344
	ds_read_b128 v[118:121], v138 offset:58368
	ds_read_b128 v[122:125], v138 offset:59392
	ds_read_b128 v[66:69], v138 offset:60416
	ds_read_b128 v[70:73], v138 offset:61440
	ds_read_b128 v[74:77], v138 offset:62464
	ds_read_b128 v[78:81], v138 offset:63488
	s_waitcnt lgkmcnt(6)
	v_mfma_f32_16x16x32_f16 v[82:85], v[114:117], v[126:129], v[82:85]
	ds_read_b128 v[114:117], v138 offset:64512
	s_waitcnt lgkmcnt(6)
	v_mfma_f32_16x16x32_f16 v[86:89], v[118:121], v[126:129], v[86:89]
	ds_read_b128 v[130:133], v137 offset:64
	ds_read_b128 v[118:121], v139
	s_waitcnt lgkmcnt(7)
	v_mfma_f32_16x16x32_f16 v[90:93], v[122:125], v[126:129], v[90:93]
	ds_read_b128 v[122:125], v139 offset:1024
	s_waitcnt lgkmcnt(7)
	v_mfma_f32_16x16x32_f16 v[94:97], v[66:69], v[126:129], v[94:97]
	ds_read_b128 v[66:69], v139 offset:2048
	s_waitcnt lgkmcnt(7)
	v_mfma_f32_16x16x32_f16 v[98:101], v[70:73], v[126:129], v[98:101]
	ds_read_b128 v[70:73], v139 offset:3072
	s_waitcnt lgkmcnt(7)
	v_mfma_f32_16x16x32_f16 v[102:105], v[74:77], v[126:129], v[102:105]
	ds_read_b128 v[74:77], v139 offset:4096
	s_waitcnt lgkmcnt(7)
	v_mfma_f32_16x16x32_f16 v[106:109], v[78:81], v[126:129], v[106:109]
	ds_read_b128 v[78:81], v139 offset:5120
	s_waitcnt lgkmcnt(7)
	v_mfma_f32_16x16x32_f16 v[110:113], v[114:117], v[126:129], v[110:113]
	ds_read_b128 v[114:117], v139 offset:6144
	s_waitcnt lgkmcnt(6)
	v_mfma_f32_16x16x32_f16 v[82:85], v[118:121], v[130:133], v[82:85]
	ds_read_b128 v[118:121], v139 offset:7168
	s_waitcnt lgkmcnt(6)
	v_mfma_f32_16x16x32_f16 v[86:89], v[122:125], v[130:133], v[86:89]
	ds_read_b128 v[126:129], v137 offset:128
	ds_read_b128 v[122:125], v139 offset:8192
	s_waitcnt lgkmcnt(7)
	v_mfma_f32_16x16x32_f16 v[90:93], v[66:69], v[130:133], v[90:93]
	ds_read_b128 v[66:69], v139 offset:9216
	s_waitcnt lgkmcnt(7)
	v_mfma_f32_16x16x32_f16 v[94:97], v[70:73], v[130:133], v[94:97]
	ds_read_b128 v[70:73], v139 offset:10240
	s_waitcnt lgkmcnt(7)
	v_mfma_f32_16x16x32_f16 v[98:101], v[74:77], v[130:133], v[98:101]
	ds_read_b128 v[74:77], v139 offset:11264
	s_waitcnt lgkmcnt(7)
	v_mfma_f32_16x16x32_f16 v[102:105], v[78:81], v[130:133], v[102:105]
	ds_read_b128 v[78:81], v139 offset:12288
	s_waitcnt lgkmcnt(7)
	v_mfma_f32_16x16x32_f16 v[106:109], v[114:117], v[130:133], v[106:109]
	ds_read_b128 v[114:117], v139 offset:13312
	s_waitcnt lgkmcnt(7)
	v_mfma_f32_16x16x32_f16 v[110:113], v[118:121], v[130:133], v[110:113]
	ds_read_b128 v[118:121], v139 offset:14336
	s_waitcnt lgkmcnt(6)
	v_mfma_f32_16x16x32_f16 v[82:85], v[122:125], v[126:129], v[82:85]
	ds_read_b128 v[122:125], v139 offset:15360
	s_waitcnt lgkmcnt(6)
	v_mfma_f32_16x16x32_f16 v[86:89], v[66:69], v[126:129], v[86:89]
	s_waitcnt lgkmcnt(5)
	v_mfma_f32_16x16x32_f16 v[90:93], v[70:73], v[126:129], v[90:93]
	s_waitcnt lgkmcnt(4)
	v_mfma_f32_16x16x32_f16 v[94:97], v[74:77], v[126:129], v[94:97]
	s_waitcnt lgkmcnt(3)
	v_mfma_f32_16x16x32_f16 v[98:101], v[78:81], v[126:129], v[98:101]
	s_waitcnt lgkmcnt(2)
	v_mfma_f32_16x16x32_f16 v[102:105], v[114:117], v[126:129], v[102:105]
	s_waitcnt lgkmcnt(1)
	v_mfma_f32_16x16x32_f16 v[106:109], v[118:121], v[126:129], v[106:109]
	s_waitcnt lgkmcnt(0)
	v_mfma_f32_16x16x32_f16 v[110:113], v[122:125], v[126:129], v[110:113]
	s_nop 7
	s_nop 3
	v_max_f32_e32 v82, 0, v82
	v_max_f32_e32 v83, 0, v83
	v_max_f32_e32 v84, 0, v84
	v_max_f32_e32 v85, 0, v85
	v_cvt_pk_f16_f32 v160, v82, v83
	v_cvt_pk_f16_f32 v161, v84, v85
	ds_write_b64 v140, v[160:161]
	v_max_f32_e32 v86, 0, v86
	v_max_f32_e32 v87, 0, v87
	v_max_f32_e32 v88, 0, v88
	v_max_f32_e32 v89, 0, v89
	v_cvt_pk_f16_f32 v162, v86, v87
	v_cvt_pk_f16_f32 v163, v88, v89
	ds_write_b64 v140, v[162:163] offset:32
	v_max_f32_e32 v90, 0, v90
	v_max_f32_e32 v91, 0, v91
	v_max_f32_e32 v92, 0, v92
	v_max_f32_e32 v93, 0, v93
	v_cvt_pk_f16_f32 v160, v90, v91
	v_cvt_pk_f16_f32 v161, v92, v93
	ds_write_b64 v140, v[160:161] offset:64
	v_max_f32_e32 v94, 0, v94
	v_max_f32_e32 v95, 0, v95
	v_max_f32_e32 v96, 0, v96
	v_max_f32_e32 v97, 0, v97
	v_cvt_pk_f16_f32 v162, v94, v95
	v_cvt_pk_f16_f32 v163, v96, v97
	ds_write_b64 v140, v[162:163] offset:96
	v_max_f32_e32 v98, 0, v98
	v_max_f32_e32 v99, 0, v99
	v_max_f32_e32 v100, 0, v100
	v_max_f32_e32 v101, 0, v101
	v_cvt_pk_f16_f32 v160, v98, v99
	v_cvt_pk_f16_f32 v161, v100, v101
	ds_write_b64 v140, v[160:161] offset:128
	v_max_f32_e32 v102, 0, v102
	v_max_f32_e32 v103, 0, v103
	v_max_f32_e32 v104, 0, v104
	v_max_f32_e32 v105, 0, v105
	v_cvt_pk_f16_f32 v162, v102, v103
	v_cvt_pk_f16_f32 v163, v104, v105
	ds_write_b64 v140, v[162:163] offset:160
	v_max_f32_e32 v106, 0, v106
	v_max_f32_e32 v107, 0, v107
	v_max_f32_e32 v108, 0, v108
	v_max_f32_e32 v109, 0, v109
	v_cvt_pk_f16_f32 v160, v106, v107
	v_cvt_pk_f16_f32 v161, v108, v109
	ds_write_b64 v140, v[160:161] offset:192
	v_max_f32_e32 v110, 0, v110
	v_max_f32_e32 v111, 0, v111
	v_max_f32_e32 v112, 0, v112
	v_max_f32_e32 v113, 0, v113
	v_cvt_pk_f16_f32 v162, v110, v111
	v_cvt_pk_f16_f32 v163, v112, v113
	ds_write_b64 v140, v[162:163] offset:224
	s_lshl_b32 s52, s33, 12
	v_add_u32_e32 v158, s52, v142
	ds_read_b128 v[114:117], v141
	ds_read_b128 v[118:121], v141 offset:1088
	ds_read_b128 v[122:125], v141 offset:2176
	ds_read_b128 v[126:129], v141 offset:3264
	s_waitcnt lgkmcnt(3)
	global_store_dwordx4 v158, v[114:117], s[22:23] sc1 nt
	s_waitcnt lgkmcnt(2)
	global_store_dwordx4 v158, v[118:121], s[22:23] offset:1024 sc1 nt
	s_waitcnt lgkmcnt(1)
	global_store_dwordx4 v158, v[122:125], s[22:23] offset:2048 sc1 nt
	s_waitcnt lgkmcnt(0)
	global_store_dwordx4 v158, v[126:129], s[22:23] offset:3072 sc1 nt
	s_nop 1
	s_mov_b32 s66, 0
	s_branch .Lfa_tilestart

.Lfb_tileend:
	s_setprio 2
	ds_read_b128 v[126:129], v137
	ds_read_b128 v[114:117], v139
	ds_read_b128 v[118:121], v139 offset:1024
	ds_read_b128 v[122:125], v139 offset:2048
	ds_read_b128 v[66:69], v139 offset:3072
	ds_read_b128 v[70:73], v139 offset:4096
	ds_read_b128 v[74:77], v139 offset:5120
	ds_read_b128 v[78:81], v139 offset:6144
	s_waitcnt lgkmcnt(6)
	v_mfma_f32_16x16x32_f16 v[82:85], v[114:117], v[126:129], v[82:85]
	ds_read_b128 v[114:117], v139 offset:7168
	s_waitcnt lgkmcnt(6)
	v_mfma_f32_16x16x32_f16 v[86:89], v[118:121], v[126:129], v[86:89]
	ds_read_b128 v[130:133], v137 offset:64
	ds_read_b128 v[118:121], v139 offset:8192
	s_waitcnt lgkmcnt(7)
	v_mfma_f32_16x16x32_f16 v[90:93], v[122:125], v[126:129], v[90:93]
	ds_read_b128 v[122:125], v139 offset:9216
	s_waitcnt lgkmcnt(7)
	v_mfma_f32_16x16x32_f16 v[94:97], v[66:69], v[126:129], v[94:97]
	ds_read_b128 v[66:69], v139 offset:10240
	s_waitcnt lgkmcnt(7)
	v_mfma_f32_16x16x32_f16 v[98:101], v[70:73], v[126:129], v[98:101]
	ds_read_b128 v[70:73], v139 offset:11264
	s_waitcnt lgkmcnt(7)
	v_mfma_f32_16x16x32_f16 v[102:105], v[74:77], v[126:129], v[102:105]
	ds_read_b128 v[74:77], v139 offset:12288
	s_waitcnt lgkmcnt(7)
	v_mfma_f32_16x16x32_f16 v[106:109], v[78:81], v[126:129], v[106:109]
	ds_read_b128 v[78:81], v139 offset:13312
	s_waitcnt lgkmcnt(7)
	v_mfma_f32_16x16x32_f16 v[110:113], v[114:117], v[126:129], v[110:113]
	ds_read_b128 v[114:117], v139 offset:14336
	s_waitcnt lgkmcnt(6)
	v_mfma_f32_16x16x32_f16 v[82:85], v[118:121], v[130:133], v[82:85]
	ds_read_b128 v[118:121], v139 offset:15360
	s_waitcnt lgkmcnt(6)
	v_mfma_f32_16x16x32_f16 v[86:89], v[122:125], v[130:133], v[86:89]
	ds_read_b128 v[126:129], v137 offset:128
	ds_read_b128 v[122:125], v139 offset:16384
	s_waitcnt lgkmcnt(7)
	v_mfma_f32_16x16x32_f16 v[90:93], v[66:69], v[130:133], v[90:93]
	ds_read_b128 v[66:69], v139 offset:17408
	s_waitcnt lgkmcnt(7)
	v_mfma_f32_16x16x32_f16 v[94:97], v[70:73], v[130:133], v[94:97]
	ds_read_b128 v[70:73], v139 offset:18432
	s_waitcnt lgkmcnt(7)
	v_mfma_f32_16x16x32_f16 v[98:101], v[74:77], v[130:133], v[98:101]
	ds_read_b128 v[74:77], v139 offset:19456
	s_waitcnt lgkmcnt(7)
	v_mfma_f32_16x16x32_f16 v[102:105], v[78:81], v[130:133], v[102:105]
	ds_read_b128 v[78:81], v139 offset:20480
	s_waitcnt lgkmcnt(7)
	v_mfma_f32_16x16x32_f16 v[106:109], v[114:117], v[130:133], v[106:109]
	ds_read_b128 v[114:117], v139 offset:21504
	s_waitcnt lgkmcnt(7)
	v_mfma_f32_16x16x32_f16 v[110:113], v[118:121], v[130:133], v[110:113]
	ds_read_b128 v[118:121], v139 offset:22528
	s_waitcnt lgkmcnt(6)
	v_mfma_f32_16x16x32_f16 v[82:85], v[122:125], v[126:129], v[82:85]
	ds_read_b128 v[122:125], v139 offset:23552
	s_waitcnt lgkmcnt(6)
	v_mfma_f32_16x16x32_f16 v[86:89], v[66:69], v[126:129], v[86:89]
	ds_read_b128 v[130:133], v137 offset:192
	ds_read_b128 v[66:69], v139 offset:24576
	s_waitcnt lgkmcnt(7)
	v_mfma_f32_16x16x32_f16 v[90:93], v[70:73], v[126:129], v[90:93]
	ds_read_b128 v[70:73], v139 offset:25600
	s_waitcnt lgkmcnt(7)
	v_mfma_f32_16x16x32_f16 v[94:97], v[74:77], v[126:129], v[94:97]
	ds_read_b128 v[74:77], v139 offset:26624
	s_waitcnt lgkmcnt(7)
	v_mfma_f32_16x16x32_f16 v[98:101], v[78:81], v[126:129], v[98:101]
	ds_read_b128 v[78:81], v139 offset:27648
	s_waitcnt lgkmcnt(7)
	v_mfma_f32_16x16x32_f16 v[102:105], v[114:117], v[126:129], v[102:105]
	ds_read_b128 v[114:117], v139 offset:28672
	s_waitcnt lgkmcnt(7)
	v_mfma_f32_16x16x32_f16 v[106:109], v[118:121], v[126:129], v[106:109]
	ds_read_b128 v[118:121], v139 offset:29696
	s_waitcnt lgkmcnt(7)
	v_mfma_f32_16x16x32_f16 v[110:113], v[122:125], v[126:129], v[110:113]
	ds_read_b128 v[122:125], v139 offset:30720
	s_waitcnt lgkmcnt(6)
	v_mfma_f32_16x16x32_f16 v[82:85], v[66:69], v[130:133], v[82:85]
	ds_read_b128 v[66:69], v139 offset:31744
	s_waitcnt lgkmcnt(6)
	v_mfma_f32_16x16x32_f16 v[86:89], v[70:73], v[130:133], v[86:89]
	s_waitcnt lgkmcnt(5)
	v_mfma_f32_16x16x32_f16 v[90:93], v[74:77], v[130:133], v[90:93]
	s_waitcnt lgkmcnt(4)
	v_mfma_f32_16x16x32_f16 v[94:97], v[78:81], v[130:133], v[94:97]
	s_waitcnt lgkmcnt(3)
	v_mfma_f32_16x16x32_f16 v[98:101], v[114:117], v[130:133], v[98:101]
	s_waitcnt lgkmcnt(2)
	v_mfma_f32_16x16x32_f16 v[102:105], v[118:121], v[130:133], v[102:105]
	s_waitcnt lgkmcnt(1)
	v_mfma_f32_16x16x32_f16 v[106:109], v[122:125], v[130:133], v[106:109]
	s_waitcnt lgkmcnt(0)
	v_mfma_f32_16x16x32_f16 v[110:113], v[66:69], v[130:133], v[110:113]
	s_nop 7
	s_nop 3
	v_max_f32_e32 v82, 0, v82
	v_max_f32_e32 v83, 0, v83
	v_max_f32_e32 v84, 0, v84
	v_max_f32_e32 v85, 0, v85
	v_cvt_pk_f16_f32 v160, v82, v83
	v_cvt_pk_f16_f32 v161, v84, v85
	ds_write_b64 v140, v[160:161]
	v_max_f32_e32 v86, 0, v86
	v_max_f32_e32 v87, 0, v87
	v_max_f32_e32 v88, 0, v88
	v_max_f32_e32 v89, 0, v89
	v_cvt_pk_f16_f32 v162, v86, v87
	v_cvt_pk_f16_f32 v163, v88, v89
	ds_write_b64 v140, v[162:163] offset:32
	v_max_f32_e32 v90, 0, v90
	v_max_f32_e32 v91, 0, v91
	v_max_f32_e32 v92, 0, v92
	v_max_f32_e32 v93, 0, v93
	v_cvt_pk_f16_f32 v160, v90, v91
	v_cvt_pk_f16_f32 v161, v92, v93
	ds_write_b64 v140, v[160:161] offset:64
	v_max_f32_e32 v94, 0, v94
	v_max_f32_e32 v95, 0, v95
	v_max_f32_e32 v96, 0, v96
	v_max_f32_e32 v97, 0, v97
	v_cvt_pk_f16_f32 v162, v94, v95
	v_cvt_pk_f16_f32 v163, v96, v97
	ds_write_b64 v140, v[162:163] offset:96
	v_max_f32_e32 v98, 0, v98
	v_max_f32_e32 v99, 0, v99
	v_max_f32_e32 v100, 0, v100
	v_max_f32_e32 v101, 0, v101
	v_cvt_pk_f16_f32 v160, v98, v99
	v_cvt_pk_f16_f32 v161, v100, v101
	ds_write_b64 v140, v[160:161] offset:128
	v_max_f32_e32 v102, 0, v102
	v_max_f32_e32 v103, 0, v103
	v_max_f32_e32 v104, 0, v104
	v_max_f32_e32 v105, 0, v105
	v_cvt_pk_f16_f32 v162, v102, v103
	v_cvt_pk_f16_f32 v163, v104, v105
	ds_write_b64 v140, v[162:163] offset:160
	v_max_f32_e32 v106, 0, v106
	v_max_f32_e32 v107, 0, v107
	v_max_f32_e32 v108, 0, v108
	v_max_f32_e32 v109, 0, v109
	v_cvt_pk_f16_f32 v160, v106, v107
	v_cvt_pk_f16_f32 v161, v108, v109
	ds_write_b64 v140, v[160:161] offset:192
	v_max_f32_e32 v110, 0, v110
	v_max_f32_e32 v111, 0, v111
	v_max_f32_e32 v112, 0, v112
	v_max_f32_e32 v113, 0, v113
	v_cvt_pk_f16_f32 v162, v110, v111
	v_cvt_pk_f16_f32 v163, v112, v113
	ds_write_b64 v140, v[162:163] offset:224
	s_lshl_b32 s52, s33, 12
	v_add_u32_e32 v158, s52, v142
	ds_read_b128 v[114:117], v141
	ds_read_b128 v[118:121], v141 offset:1088
	ds_read_b128 v[122:125], v141 offset:2176
	ds_read_b128 v[126:129], v141 offset:3264
	s_waitcnt lgkmcnt(3)
	global_store_dwordx4 v158, v[114:117], s[22:23] sc1 nt
	s_waitcnt lgkmcnt(2)
	global_store_dwordx4 v158, v[118:121], s[22:23] offset:1024 sc1 nt
	s_waitcnt lgkmcnt(1)
	global_store_dwordx4 v158, v[122:125], s[22:23] offset:2048 sc1 nt
	s_waitcnt lgkmcnt(0)
	global_store_dwordx4 v158, v[126:129], s[22:23] offset:3072 sc1 nt
	s_nop 1
	s_mov_b32 s66, 0
	s_branch .Lfb_tilestart
